# v40 + out-of-line first-iteration blocks + per-phase s_setprio flips removed
# baseline (speedup 1.0000x reference)
.LBB4_22:
	s_mov_b32 m0, s70
	ds_read_b128 v[130:133], v136 offset:16384
	ds_read_b128 v[142:145], v136 offset:17408
	ds_read_b128 v[146:149], v136 offset:18432
	ds_read_b128 v[150:153], v136 offset:19456
	ds_read_b128 v[154:157], v137
	ds_read_b128 v[158:161], v137 offset:1024
	ds_read_b128 v[162:165], v137 offset:2048
	ds_read_b128 v[166:169], v137 offset:3072
	ds_read_b128 v[170:173], v137 offset:4096
	ds_read_b128 v[174:177], v137 offset:5120
	ds_read_b128 v[178:181], v137 offset:6144
	ds_read_b128 v[182:185], v137 offset:7168
	global_load_lds_dwordx4 v0, s[74:75]
	s_add_i32 m0, s70, 0x2000
	s_nop 0
	global_load_lds_dwordx4 v120, s[74:75]
	s_barrier
	s_waitcnt lgkmcnt(7)
	v_mfma_f32_16x16x32_f16 v[94:97], v[130:133], v[154:157], v[94:97]
	v_mfma_f32_16x16x32_f16 v[90:93], v[146:149], v[154:157], v[90:93]
	s_waitcnt lgkmcnt(5)
	v_mfma_f32_16x16x32_f16 v[82:85], v[130:133], v[162:165], v[82:85]
	v_mfma_f32_16x16x32_f16 v[78:81], v[146:149], v[162:165], v[78:81]
	s_waitcnt lgkmcnt(3)
	v_mfma_f32_16x16x32_f16 v[70:73], v[130:133], v[170:173], v[70:73]
	v_mfma_f32_16x16x32_f16 v[66:69], v[146:149], v[170:173], v[66:69]
	s_waitcnt lgkmcnt(1)
	v_mfma_f32_16x16x32_f16 v[58:61], v[130:133], v[178:181], v[58:61]
	v_mfma_f32_16x16x32_f16 v[54:57], v[146:149], v[178:181], v[54:57]
	v_mfma_f32_16x16x32_f16 v[94:97], v[142:145], v[158:161], v[94:97]
	v_mfma_f32_16x16x32_f16 v[90:93], v[150:153], v[158:161], v[90:93]
	v_mfma_f32_16x16x32_f16 v[82:85], v[142:145], v[166:169], v[82:85]
	v_mfma_f32_16x16x32_f16 v[78:81], v[150:153], v[166:169], v[78:81]
	v_mfma_f32_16x16x32_f16 v[70:73], v[142:145], v[174:177], v[70:73]
	v_mfma_f32_16x16x32_f16 v[66:69], v[150:153], v[174:177], v[66:69]
	s_waitcnt lgkmcnt(0)
	v_mfma_f32_16x16x32_f16 v[58:61], v[142:145], v[182:185], v[58:61]
	v_mfma_f32_16x16x32_f16 v[54:57], v[150:153], v[182:185], v[54:57]
	s_barrier
	s_add_i32 m0, s49, 0x18000
	ds_read_b128 v[130:133], v136 offset:20480
	ds_read_b128 v[142:145], v136 offset:21504
	global_load_lds_dwordx4 v122, s[76:77]
	s_add_i32 m0, s49, 0x1a000
	s_nop 0
	global_load_lds_dwordx4 v124, s[76:77]
	s_add_i32 m0, s49, 0x1c000
	s_nop 0
	global_load_lds_dwordx4 v126, s[76:77]
	s_cmp_eq_u32 s67, 0
	s_cbranch_scc1 .Lpj_first_0
	s_waitcnt vmcnt(5)
.Lpj_join_0:
	s_barrier
	s_waitcnt lgkmcnt(1)
	v_mfma_f32_16x16x32_f16 v[86:89], v[130:133], v[154:157], v[86:89]
	v_mfma_f32_16x16x32_f16 v[74:77], v[130:133], v[162:165], v[74:77]
	v_mfma_f32_16x16x32_f16 v[62:65], v[130:133], v[170:173], v[62:65]
	v_mfma_f32_16x16x32_f16 v[50:53], v[130:133], v[178:181], v[50:53]
	s_waitcnt lgkmcnt(0)
	v_mfma_f32_16x16x32_f16 v[86:89], v[142:145], v[158:161], v[86:89]
	v_mfma_f32_16x16x32_f16 v[74:77], v[142:145], v[166:169], v[74:77]
	v_mfma_f32_16x16x32_f16 v[62:65], v[142:145], v[174:177], v[62:65]
	v_mfma_f32_16x16x32_f16 v[50:53], v[142:145], v[182:185], v[50:53]
	s_barrier
	s_mov_b32 m0, s49
	ds_read_b128 v[130:133], v136 offset:57344
	ds_read_b128 v[142:145], v136 offset:58368
	ds_read_b128 v[146:149], v136 offset:59392
	ds_read_b128 v[150:153], v136 offset:60416
	ds_read_b128 v[154:157], v137 offset:40960
	ds_read_b128 v[158:161], v137 offset:41984
	ds_read_b128 v[162:165], v137 offset:43008
	ds_read_b128 v[166:169], v137 offset:44032
	ds_read_b128 v[170:173], v137 offset:45056
	ds_read_b128 v[174:177], v137 offset:46080
	ds_read_b128 v[178:181], v137 offset:47104
	ds_read_b128 v[182:185], v137 offset:48128
	global_load_lds_dwordx4 v110, s[68:69]
	s_mov_b32 m0, s50
	s_nop 0
	global_load_lds_dwordx4 v114, s[68:69]
	s_barrier
	s_waitcnt lgkmcnt(7)
	v_mfma_f32_16x16x32_f16 v[94:97], v[130:133], v[154:157], v[94:97]
	v_mfma_f32_16x16x32_f16 v[90:93], v[146:149], v[154:157], v[90:93]
	s_waitcnt lgkmcnt(5)
	v_mfma_f32_16x16x32_f16 v[82:85], v[130:133], v[162:165], v[82:85]
	v_mfma_f32_16x16x32_f16 v[78:81], v[146:149], v[162:165], v[78:81]
	s_waitcnt lgkmcnt(3)
	v_mfma_f32_16x16x32_f16 v[70:73], v[130:133], v[170:173], v[70:73]
	v_mfma_f32_16x16x32_f16 v[66:69], v[146:149], v[170:173], v[66:69]
	s_waitcnt lgkmcnt(1)
	v_mfma_f32_16x16x32_f16 v[58:61], v[130:133], v[178:181], v[58:61]
	v_mfma_f32_16x16x32_f16 v[54:57], v[146:149], v[178:181], v[54:57]
	v_mfma_f32_16x16x32_f16 v[94:97], v[142:145], v[158:161], v[94:97]
	v_mfma_f32_16x16x32_f16 v[90:93], v[150:153], v[158:161], v[90:93]
	v_mfma_f32_16x16x32_f16 v[82:85], v[142:145], v[166:169], v[82:85]
	v_mfma_f32_16x16x32_f16 v[78:81], v[150:153], v[166:169], v[78:81]
	v_mfma_f32_16x16x32_f16 v[70:73], v[142:145], v[174:177], v[70:73]
	v_mfma_f32_16x16x32_f16 v[66:69], v[150:153], v[174:177], v[66:69]
	s_waitcnt lgkmcnt(0)
	v_mfma_f32_16x16x32_f16 v[58:61], v[142:145], v[182:185], v[58:61]
	v_mfma_f32_16x16x32_f16 v[54:57], v[150:153], v[182:185], v[54:57]
	s_barrier
	s_mov_b32 m0, s51
	ds_read_b128 v[130:133], v136 offset:61440
	ds_read_b128 v[142:145], v136 offset:62464
	global_load_lds_dwordx4 v112, s[34:35]
	s_mov_b32 m0, s52
	s_nop 0
	global_load_lds_dwordx4 v116, s[34:35]
	s_mov_b32 m0, s53
	s_nop 0
	global_load_lds_dwordx4 v118, s[34:35]
	s_cmp_eq_u32 s67, 0
	s_cbranch_scc1 .Lpj_first_1
	s_waitcnt vmcnt(5)
.Lpj_join_1:
	s_barrier
	s_waitcnt lgkmcnt(1)
	v_mfma_f32_16x16x32_f16 v[86:89], v[130:133], v[154:157], v[86:89]
	v_mfma_f32_16x16x32_f16 v[74:77], v[130:133], v[162:165], v[74:77]
	v_mfma_f32_16x16x32_f16 v[62:65], v[130:133], v[170:173], v[62:65]
	v_mfma_f32_16x16x32_f16 v[50:53], v[130:133], v[178:181], v[50:53]
	s_waitcnt lgkmcnt(0)
	v_mfma_f32_16x16x32_f16 v[86:89], v[142:145], v[158:161], v[86:89]
	v_mfma_f32_16x16x32_f16 v[74:77], v[142:145], v[166:169], v[74:77]
	v_mfma_f32_16x16x32_f16 v[62:65], v[142:145], v[174:177], v[62:65]
	v_mfma_f32_16x16x32_f16 v[50:53], v[142:145], v[182:185], v[50:53]
	s_barrier
	s_mov_b32 m0, s56
	ds_read_b128 v[130:133], v138
	ds_read_b128 v[142:145], v138 offset:1024
	ds_read_b128 v[146:149], v138 offset:2048
	ds_read_b128 v[150:153], v138 offset:3072
	ds_read_b128 v[154:157], v139
	ds_read_b128 v[158:161], v139 offset:1024
	ds_read_b128 v[162:165], v139 offset:2048
	ds_read_b128 v[166:169], v139 offset:3072
	ds_read_b128 v[170:173], v139 offset:4096
	ds_read_b128 v[174:177], v139 offset:5120
	ds_read_b128 v[178:181], v139 offset:6144
	ds_read_b128 v[182:185], v139 offset:7168
	global_load_lds_dwordx4 v110, s[78:79]
	s_mov_b32 m0, s57
	s_nop 0
	global_load_lds_dwordx4 v114, s[78:79]
	s_barrier
	s_waitcnt lgkmcnt(7)
	v_mfma_f32_16x16x32_f16 v[94:97], v[130:133], v[154:157], v[94:97]
	v_mfma_f32_16x16x32_f16 v[90:93], v[146:149], v[154:157], v[90:93]
	s_waitcnt lgkmcnt(5)
	v_mfma_f32_16x16x32_f16 v[82:85], v[130:133], v[162:165], v[82:85]
	v_mfma_f32_16x16x32_f16 v[78:81], v[146:149], v[162:165], v[78:81]
	s_waitcnt lgkmcnt(3)
	v_mfma_f32_16x16x32_f16 v[70:73], v[130:133], v[170:173], v[70:73]
	v_mfma_f32_16x16x32_f16 v[66:69], v[146:149], v[170:173], v[66:69]
	s_waitcnt lgkmcnt(1)
	v_mfma_f32_16x16x32_f16 v[58:61], v[130:133], v[178:181], v[58:61]
	v_mfma_f32_16x16x32_f16 v[54:57], v[146:149], v[178:181], v[54:57]
	v_mfma_f32_16x16x32_f16 v[94:97], v[142:145], v[158:161], v[94:97]
	v_mfma_f32_16x16x32_f16 v[90:93], v[150:153], v[158:161], v[90:93]
	v_mfma_f32_16x16x32_f16 v[82:85], v[142:145], v[166:169], v[82:85]
	v_mfma_f32_16x16x32_f16 v[78:81], v[150:153], v[166:169], v[78:81]
	v_mfma_f32_16x16x32_f16 v[70:73], v[142:145], v[174:177], v[70:73]
	v_mfma_f32_16x16x32_f16 v[66:69], v[150:153], v[174:177], v[66:69]
	s_waitcnt lgkmcnt(0)
	v_mfma_f32_16x16x32_f16 v[58:61], v[142:145], v[182:185], v[58:61]
	v_mfma_f32_16x16x32_f16 v[54:57], v[150:153], v[182:185], v[54:57]
	s_barrier
	s_mov_b32 m0, s58
	ds_read_b128 v[130:133], v138 offset:4096
	ds_read_b128 v[142:145], v138 offset:5120
	global_load_lds_dwordx4 v112, s[80:81]
	s_add_i32 m0, s58, 0x2000
	s_nop 0
	global_load_lds_dwordx4 v116, s[80:81]
	s_add_i32 m0, s58, 0x4000
	s_nop 0
	global_load_lds_dwordx4 v118, s[80:81]
	s_cmp_eq_u32 s67, 0
	s_cbranch_scc1 .Lpj_first_2
	s_waitcnt vmcnt(5)

.LBB6_22:
	s_mov_b32 m0, s68
	ds_read_b128 v[132:135], v131 offset:16384
	ds_read_b128 v[136:139], v131 offset:17408
	ds_read_b128 v[140:143], v131 offset:18432
	ds_read_b128 v[144:147], v131 offset:19456
	ds_read_b128 v[148:151], v182
	ds_read_b128 v[152:155], v182 offset:1024
	ds_read_b128 v[156:159], v182 offset:2048
	ds_read_b128 v[160:163], v182 offset:3072
	ds_read_b128 v[164:167], v182 offset:4096
	ds_read_b128 v[168:171], v182 offset:5120
	ds_read_b128 v[172:175], v182 offset:6144
	ds_read_b128 v[176:179], v182 offset:7168
	global_load_lds_dwordx4 v106, s[72:73]
	s_add_i32 m0, s68, 0x2000
	s_nop 0
	global_load_lds_dwordx4 v108, s[72:73]
	s_barrier
	s_waitcnt lgkmcnt(7)
	v_mfma_f32_16x16x32_f16 v[40:43], v[132:135], v[148:151], v[40:43]
	v_mfma_f32_16x16x32_f16 v[44:47], v[140:143], v[148:151], v[44:47]
	s_waitcnt lgkmcnt(5)
	v_mfma_f32_16x16x32_f16 v[32:35], v[132:135], v[156:159], v[32:35]
	v_mfma_f32_16x16x32_f16 v[28:31], v[140:143], v[156:159], v[28:31]
	s_waitcnt lgkmcnt(3)
	v_mfma_f32_16x16x32_f16 v[20:23], v[132:135], v[164:167], v[20:23]
	v_mfma_f32_16x16x32_f16 v[16:19], v[140:143], v[164:167], v[16:19]
	s_waitcnt lgkmcnt(1)
	v_mfma_f32_16x16x32_f16 v[8:11], v[132:135], v[172:175], v[8:11]
	v_mfma_f32_16x16x32_f16 v[4:7], v[140:143], v[172:175], v[4:7]
	v_mfma_f32_16x16x32_f16 v[40:43], v[136:139], v[152:155], v[40:43]
	v_mfma_f32_16x16x32_f16 v[44:47], v[144:147], v[152:155], v[44:47]
	v_mfma_f32_16x16x32_f16 v[32:35], v[136:139], v[160:163], v[32:35]
	v_mfma_f32_16x16x32_f16 v[28:31], v[144:147], v[160:163], v[28:31]
	v_mfma_f32_16x16x32_f16 v[20:23], v[136:139], v[168:171], v[20:23]
	v_mfma_f32_16x16x32_f16 v[16:19], v[144:147], v[168:171], v[16:19]
	s_waitcnt lgkmcnt(0)
	v_mfma_f32_16x16x32_f16 v[8:11], v[136:139], v[176:179], v[8:11]
	v_mfma_f32_16x16x32_f16 v[4:7], v[144:147], v[176:179], v[4:7]
	s_barrier
	s_add_i32 m0, s47, 0x18000
	ds_read_b128 v[132:135], v131 offset:20480
	ds_read_b128 v[136:139], v131 offset:21504
	global_load_lds_dwordx4 v110, s[74:75]
	s_add_i32 m0, s47, 0x1a000
	s_nop 0
	global_load_lds_dwordx4 v112, s[74:75]
	s_add_i32 m0, s47, 0x1c000
	s_nop 0
	global_load_lds_dwordx4 v114, s[74:75]
	s_cmp_eq_u32 s65, 0
	s_cbranch_scc1 .Lm2_first_0
	s_waitcnt vmcnt(5)
.Lm2_join_0:
	s_barrier
	s_waitcnt lgkmcnt(1)
	v_mfma_f32_16x16x32_f16 v[36:39], v[132:135], v[148:151], v[36:39]
	v_mfma_f32_16x16x32_f16 v[24:27], v[132:135], v[156:159], v[24:27]
	v_mfma_f32_16x16x32_f16 v[12:15], v[132:135], v[164:167], v[12:15]
	v_mfma_f32_16x16x32_f16 v[0:3], v[132:135], v[172:175], v[0:3]
	s_waitcnt lgkmcnt(0)
	v_mfma_f32_16x16x32_f16 v[36:39], v[136:139], v[152:155], v[36:39]
	v_mfma_f32_16x16x32_f16 v[24:27], v[136:139], v[160:163], v[24:27]
	v_mfma_f32_16x16x32_f16 v[12:15], v[136:139], v[168:171], v[12:15]
	v_mfma_f32_16x16x32_f16 v[0:3], v[136:139], v[176:179], v[0:3]
	s_barrier
	s_mov_b32 m0, s47
	ds_read_b128 v[132:135], v131 offset:57344
	ds_read_b128 v[136:139], v131 offset:58368
	ds_read_b128 v[140:143], v131 offset:59392
	ds_read_b128 v[144:147], v131 offset:60416
	ds_read_b128 v[148:151], v182 offset:40960
	ds_read_b128 v[152:155], v182 offset:41984
	ds_read_b128 v[156:159], v182 offset:43008
	ds_read_b128 v[160:163], v182 offset:44032
	ds_read_b128 v[164:167], v182 offset:45056
	ds_read_b128 v[168:171], v182 offset:46080
	ds_read_b128 v[172:175], v182 offset:47104
	ds_read_b128 v[176:179], v182 offset:48128
	global_load_lds_dwordx4 v48, s[66:67]
	s_mov_b32 m0, s48
	s_nop 0
	global_load_lds_dwordx4 v52, s[66:67]
	s_barrier
	s_waitcnt lgkmcnt(7)
	v_mfma_f32_16x16x32_f16 v[40:43], v[132:135], v[148:151], v[40:43]
	v_mfma_f32_16x16x32_f16 v[44:47], v[140:143], v[148:151], v[44:47]
	s_waitcnt lgkmcnt(5)
	v_mfma_f32_16x16x32_f16 v[32:35], v[132:135], v[156:159], v[32:35]
	v_mfma_f32_16x16x32_f16 v[28:31], v[140:143], v[156:159], v[28:31]
	s_waitcnt lgkmcnt(3)
	v_mfma_f32_16x16x32_f16 v[20:23], v[132:135], v[164:167], v[20:23]
	v_mfma_f32_16x16x32_f16 v[16:19], v[140:143], v[164:167], v[16:19]
	s_waitcnt lgkmcnt(1)
	v_mfma_f32_16x16x32_f16 v[8:11], v[132:135], v[172:175], v[8:11]
	v_mfma_f32_16x16x32_f16 v[4:7], v[140:143], v[172:175], v[4:7]
	v_mfma_f32_16x16x32_f16 v[40:43], v[136:139], v[152:155], v[40:43]
	v_mfma_f32_16x16x32_f16 v[44:47], v[144:147], v[152:155], v[44:47]
	v_mfma_f32_16x16x32_f16 v[32:35], v[136:139], v[160:163], v[32:35]
	v_mfma_f32_16x16x32_f16 v[28:31], v[144:147], v[160:163], v[28:31]
	v_mfma_f32_16x16x32_f16 v[20:23], v[136:139], v[168:171], v[20:23]
	v_mfma_f32_16x16x32_f16 v[16:19], v[144:147], v[168:171], v[16:19]
	s_waitcnt lgkmcnt(0)
	v_mfma_f32_16x16x32_f16 v[8:11], v[136:139], v[176:179], v[8:11]
	v_mfma_f32_16x16x32_f16 v[4:7], v[144:147], v[176:179], v[4:7]
	s_barrier
	s_mov_b32 m0, s49
	ds_read_b128 v[132:135], v131 offset:61440
	ds_read_b128 v[136:139], v131 offset:62464
	global_load_lds_dwordx4 v50, s[30:31]
	s_mov_b32 m0, s50
	s_nop 0
	global_load_lds_dwordx4 v54, s[30:31]
	s_mov_b32 m0, s51
	s_nop 0
	global_load_lds_dwordx4 v56, s[30:31]
	s_cmp_eq_u32 s65, 0
	s_cbranch_scc1 .Lm2_first_1
	s_waitcnt vmcnt(5)
.Lm2_join_1:
	s_barrier
	s_waitcnt lgkmcnt(1)
	v_mfma_f32_16x16x32_f16 v[36:39], v[132:135], v[148:151], v[36:39]
	v_mfma_f32_16x16x32_f16 v[24:27], v[132:135], v[156:159], v[24:27]
	v_mfma_f32_16x16x32_f16 v[12:15], v[132:135], v[164:167], v[12:15]
	v_mfma_f32_16x16x32_f16 v[0:3], v[132:135], v[172:175], v[0:3]
	s_waitcnt lgkmcnt(0)
	v_mfma_f32_16x16x32_f16 v[36:39], v[136:139], v[152:155], v[36:39]
	v_mfma_f32_16x16x32_f16 v[24:27], v[136:139], v[160:163], v[24:27]
	v_mfma_f32_16x16x32_f16 v[12:15], v[136:139], v[168:171], v[12:15]
	v_mfma_f32_16x16x32_f16 v[0:3], v[136:139], v[176:179], v[0:3]
	s_barrier
	s_mov_b32 m0, s54
	v_add_u32_e32 v131, s62, v127
	ds_read_b128 v[132:135], v130
	ds_read_b128 v[136:139], v130 offset:1024
	ds_read_b128 v[140:143], v130 offset:2048
	ds_read_b128 v[144:147], v130 offset:3072
	ds_read_b128 v[148:151], v131
	ds_read_b128 v[152:155], v131 offset:1024
	ds_read_b128 v[156:159], v131 offset:2048
	ds_read_b128 v[160:163], v131 offset:3072
	ds_read_b128 v[164:167], v131 offset:4096
	ds_read_b128 v[168:171], v131 offset:5120
	ds_read_b128 v[172:175], v131 offset:6144
	ds_read_b128 v[176:179], v131 offset:7168
	global_load_lds_dwordx4 v48, s[76:77]
	s_mov_b32 m0, s55
	s_nop 0
	global_load_lds_dwordx4 v52, s[76:77]
	s_barrier
	s_waitcnt lgkmcnt(7)
	v_mfma_f32_16x16x32_f16 v[40:43], v[132:135], v[148:151], v[40:43]
	v_mfma_f32_16x16x32_f16 v[44:47], v[140:143], v[148:151], v[44:47]
	s_waitcnt lgkmcnt(5)
	v_mfma_f32_16x16x32_f16 v[32:35], v[132:135], v[156:159], v[32:35]
	v_mfma_f32_16x16x32_f16 v[28:31], v[140:143], v[156:159], v[28:31]
	s_waitcnt lgkmcnt(3)
	v_mfma_f32_16x16x32_f16 v[20:23], v[132:135], v[164:167], v[20:23]
	v_mfma_f32_16x16x32_f16 v[16:19], v[140:143], v[164:167], v[16:19]
	s_waitcnt lgkmcnt(1)
	v_mfma_f32_16x16x32_f16 v[8:11], v[132:135], v[172:175], v[8:11]
	v_mfma_f32_16x16x32_f16 v[4:7], v[140:143], v[172:175], v[4:7]
	v_mfma_f32_16x16x32_f16 v[40:43], v[136:139], v[152:155], v[40:43]
	v_mfma_f32_16x16x32_f16 v[44:47], v[144:147], v[152:155], v[44:47]
	v_mfma_f32_16x16x32_f16 v[32:35], v[136:139], v[160:163], v[32:35]
	v_mfma_f32_16x16x32_f16 v[28:31], v[144:147], v[160:163], v[28:31]
	v_mfma_f32_16x16x32_f16 v[20:23], v[136:139], v[168:171], v[20:23]
	v_mfma_f32_16x16x32_f16 v[16:19], v[144:147], v[168:171], v[16:19]
	s_waitcnt lgkmcnt(0)
	v_mfma_f32_16x16x32_f16 v[8:11], v[136:139], v[176:179], v[8:11]
	v_mfma_f32_16x16x32_f16 v[4:7], v[144:147], v[176:179], v[4:7]
	s_barrier
	s_mov_b32 m0, s56
	ds_read_b128 v[132:135], v130 offset:4096
	ds_read_b128 v[136:139], v130 offset:5120
	global_load_lds_dwordx4 v50, s[78:79]
	s_add_i32 m0, s56, 0x2000
	s_nop 0
	global_load_lds_dwordx4 v54, s[78:79]
	s_add_i32 m0, s56, 0x4000
	s_nop 0
	global_load_lds_dwordx4 v56, s[78:79]
	s_cmp_eq_u32 s65, 0
	s_cbranch_scc1 .Lm2_first_2
	s_waitcnt vmcnt(5)
